# router phase: barrier before it becomes arrive-only; its completion is awaited after the P6-independent table/weight prep, before the first x1 load
# speedup vs baseline: 1.0257x; 1.0048x over previous
.LBB0_650:
	s_or_b64 exec, exec, s[0:1]
	v_readfirstlane_b32 s100, v186
	s_nop 0
	s_cmp_lg_u32 s100, 0
	s_cbranch_scc1 .Lp7_w_skip
	s_cmp_eq_u32 s98, 0
	s_cbranch_scc1 .Lp7_w_skip
	v_readlane_b32 s100, v235, 7
	v_readlane_b32 s101, v235, 8
	v_mov_b32_e32 v236, 0x3400
	s_nop 3
.Lp7_w_poll:
	global_load_dword v237, v236, s[100:101] sc1
	s_waitcnt vmcnt(0)
	v_readfirstlane_b32 s99, v237
	s_nop 0
	s_cmp_ge_u32 s99, s98
	s_cbranch_scc1 .Lp7_w_ok
	s_sleep 1
	s_branch .Lp7_w_poll

.Lp7_w_skip:
	s_barrier
	s_lshl_b32 s33, s56, 6
	v_add_u32_e32 v46, s33, v103
	v_ashrrev_i32_e32 v47, 31, v46
	v_or_b32_e32 v2, 1, v46
	v_lshlrev_b64 v[0:1], 11, v[46:47]
	v_ashrrev_i32_e32 v3, 31, v2
	v_lshl_add_u64 v[0:1], v[36:37], 0, v[0:1]
	v_lshlrev_b64 v[2:3], 11, v[2:3]
	v_lshl_add_u64 v[2:3], v[36:37], 0, v[2:3]
	global_load_dwordx2 v[48:49], v[0:1], off
	global_load_dwordx2 v[50:51], v[0:1], off offset:512
	global_load_dwordx2 v[54:55], v[0:1], off offset:1024
	global_load_dwordx2 v[82:83], v[0:1], off offset:1536
	global_load_dwordx2 v[52:53], v[2:3], off
	global_load_dwordx2 v[56:57], v[2:3], off offset:512
	global_load_dwordx2 v[58:59], v[2:3], off offset:1024
	global_load_dwordx2 v[60:61], v[2:3], off offset:1536
	ds_read_b128 v[0:3], v101
	ds_read_b128 v[4:7], v101 offset:1024
	ds_read_b128 v[8:11], v102
	ds_read_b128 v[12:15], v102 offset:1024
	ds_read_b128 v[16:19], v101 offset:2048
	ds_read_b128 v[20:23], v101 offset:3072
	ds_read_b128 v[24:27], v102 offset:2048
	ds_read_b128 v[28:31], v102 offset:3072
	s_mov_b32 s34, 2
	v_mov_b32_e32 v34, v110
	s_branch .LBB0_652
